# speedup vs baseline: 1.0028x; 1.0028x over previous
_Z10knn_selectPKiPKfS2_S2_Pf:
	s_load_dwordx2 s[4:5], s[0:1], 0x0
	s_load_dwordx2 s[30:31], s[0:1], 0x10
	s_load_dwordx2 s[32:33], s[0:1], 0x18
	s_load_dwordx2 s[34:35], s[0:1], 0x20
	s_mul_i32 s6, s2, 0x30e0
	s_mul_hi_i32 s3, s2, 0x30e0
	v_bfrev_b32_e32 v26, 1
	v_lshlrev_b32_e32 v1, 4, v0
	s_waitcnt lgkmcnt(0)
	s_add_u32 s4, s4, s6
	s_addc_u32 s5, s5, s3
	s_movk_i32 s3, 0x30e
	v_cmp_gt_u32_e64 s[10:11], s3, v0
	v_bfrev_b32_e32 v30, 1
	v_bfrev_b32_e32 v31, 1
	v_bfrev_b32_e32 v32, 1
	v_bfrev_b32_e32 v33, 1
	s_and_saveexec_b64 s[6:7], s[10:11]
	s_cbranch_execz .LBB2_2
	global_load_dwordx4 v[30:33], v1, s[4:5]

.LBB2_356:
	s_or_b64 exec, exec, s[8:9]
	s_waitcnt vmcnt(3)
	v_cvt_f64_f32_e32 v[38:39], v15
	s_waitcnt vmcnt(2)
	v_cvt_f64_f32_e32 v[46:47], v11
	v_cvt_f64_f32_e32 v[36:37], v14
	v_mul_f64 v[14:15], v[38:39], v[38:39]
	v_cvt_f64_f32_e32 v[44:45], v10
	v_mul_f64 v[10:11], v[46:47], v[46:47]
	s_waitcnt vmcnt(1)
	v_cvt_f64_f32_e32 v[54:55], v7
	v_fmac_f64_e32 v[14:15], v[36:37], v[36:37]
	v_cvt_f64_f32_e32 v[40:41], v16
	v_fmac_f64_e32 v[10:11], v[44:45], v[44:45]
	v_cvt_f64_f32_e32 v[48:49], v12
	v_cvt_f64_f32_e32 v[52:53], v6
	v_mul_f64 v[6:7], v[54:55], v[54:55]
	s_waitcnt vmcnt(0)
	v_cvt_f64_f32_e32 v[62:63], v3
	v_fmac_f64_e32 v[14:15], v[40:41], v[40:41]
	v_cvt_f64_f32_e32 v[42:43], v17
	v_fmac_f64_e32 v[10:11], v[48:49], v[48:49]
	v_cvt_f64_f32_e32 v[50:51], v13
	v_fmac_f64_e32 v[6:7], v[52:53], v[52:53]
	v_cvt_f64_f32_e32 v[56:57], v8
	v_cvt_f64_f32_e32 v[60:61], v2
	v_mul_f64 v[2:3], v[62:63], v[62:63]
	v_fmac_f64_e32 v[14:15], v[42:43], v[42:43]
	v_fmac_f64_e32 v[10:11], v[50:51], v[50:51]
	v_fmac_f64_e32 v[6:7], v[56:57], v[56:57]
	v_cvt_f64_f32_e32 v[58:59], v9
	v_fmac_f64_e32 v[2:3], v[60:61], v[60:61]
	v_cvt_f64_f32_e32 v[64:65], v4
	v_add_f64 v[10:11], v[14:15], v[10:11]
	v_fmac_f64_e32 v[6:7], v[58:59], v[58:59]
	v_fmac_f64_e32 v[2:3], v[64:65], v[64:65]
	v_cvt_f64_f32_e32 v[66:67], v5
	v_add_f64 v[6:7], v[10:11], v[6:7]
	v_fmac_f64_e32 v[2:3], v[66:67], v[66:67]
	v_add_f64 v[2:3], v[6:7], v[2:3]
	ds_bpermute_b32 v4, v89, v2
	ds_bpermute_b32 v5, v89, v3
	v_mov_b32_e32 v35, 0
	s_waitcnt lgkmcnt(0)
	s_barrier
	v_add_f64 v[2:3], v[2:3], v[4:5]
	ds_bpermute_b32 v4, v88, v2
	ds_bpermute_b32 v5, v88, v3
	ds_read_b64 v[72:73], v35 offset:6744
	s_mov_b64 s[8:9], s[34:35]
	s_mov_b64 s[14:15], s[30:31]
	s_waitcnt lgkmcnt(0)
	v_add_f64 v[2:3], v[2:3], v[4:5]
	ds_bpermute_b32 v4, v87, v2
	ds_bpermute_b32 v5, v87, v3
	v_readfirstlane_b32 s6, v72
	s_min_i32 s22, s6, 0x180
	v_mul_u32_u24_e32 v72, 3, v74
	v_cmp_gt_i32_e32 vcc, s22, v72
	s_waitcnt lgkmcnt(0)
	v_add_f64 v[2:3], v[2:3], v[4:5]
	ds_bpermute_b32 v4, v86, v2
	ds_bpermute_b32 v5, v86, v3
	s_waitcnt lgkmcnt(0)
	v_add_f64 v[2:3], v[2:3], v[4:5]
	ds_bpermute_b32 v4, v85, v2
	ds_bpermute_b32 v5, v85, v3
	s_waitcnt lgkmcnt(0)
	v_add_f64 v[68:69], v[2:3], v[4:5]
	ds_bpermute_b32 v70, v84, v68
	ds_bpermute_b32 v71, v84, v69
	s_and_saveexec_b64 s[6:7], vcc
	s_cbranch_execz .LBB2_365
	s_mov_b32 s12, 0
	s_add_i32 s18, s22, -1
	v_lshl_add_u64 v[74:75], s[14:15], 0, v[34:35]
	v_lshlrev_b32_e32 v35, 3, v72
	s_mov_b64 s[10:11], 0
	s_brev_b32 s13, 8
	v_mov_b32_e32 v90, 0x260
	v_mov_b32_e32 v91, 0x100
	v_mov_b32_e32 v92, 0xffffff80
	v_mov_b32_e32 v93, v72
	s_branch .LBB2_359

.LBB2_365:
	s_or_b64 exec, exec, s[6:7]
	s_mov_b64 s[12:13], s[32:33]
	s_lshl_b64 s[10:11], s[2:3], 10
	v_cmp_gt_i32_e32 vcc, s22, v0
	s_waitcnt lgkmcnt(0)
	s_barrier
	s_cmp_gt_i32 s22, 16
	s_cbranch_scc1 .Lrank1_slow
	v_lshrrev_b32_e32 v2, 4, v0
	v_and_b32_e32 v3, 15, v0
	v_lshlrev_b32_e32 v4, 3, v2
	v_lshlrev_b32_e32 v5, 3, v3
	ds_read_b64 v[6:7], v4
	ds_read_b64 v[8:9], v5
	v_lshlrev_b32_e32 v4, 2, v2
	v_lshlrev_b32_e32 v5, 2, v3
	ds_read_b32 v10, v4 offset:3072
	ds_read_b32 v11, v5 offset:3072
	v_and_b32_e32 v12, 63, v0
	v_lshrrev_b32_e32 v12, 4, v12
	s_waitcnt lgkmcnt(0)
	v_cmp_gt_f64_e64 s[0:1], v[8:9], v[6:7]
	v_cmp_eq_f64_e64 s[2:3], v[8:9], v[6:7]
	v_cmp_lt_i32_e64 s[4:5], v11, v10
	v_cmp_gt_i32_e64 s[18:19], s22, v3
	s_and_b64 s[2:3], s[2:3], s[4:5]
	s_or_b64 s[0:1], s[0:1], s[2:3]
	s_and_b64 s[0:1], s[0:1], s[18:19]
	v_mov_b32_e32 v13, s0
	v_mov_b32_e32 v14, s1
	v_cmp_lt_u32_e64 s[2:3], 1, v12
	v_and_b32_e32 v12, 1, v12
	v_lshlrev_b32_e32 v12, 4, v12
	v_cndmask_b32_e64 v13, v13, v14, s[2:3]
	v_lshrrev_b32_e32 v13, v12, v13
	v_and_b32_e32 v13, 0xffff, v13
	v_bcnt_u32_b32 v13, v13, 0
	v_cmp_gt_i32_e64 s[2:3], s22, v2
	v_cmp_eq_u32_e64 s[4:5], 0, v3
	s_and_b64 s[2:3], s[2:3], s[4:5]
	v_cmp_eq_u32_e64 s[0:1], 3, v13
	s_and_b64 s[0:1], s[0:1], s[2:3]
	s_mov_b64 s[16:17], exec
	s_and_b64 exec, exec, s[0:1]
	v_mov_b32_e32 v12, 0
	ds_write_b64 v12, v[6:7] offset:6736
	s_branch .LBB2_395

	.amdhsa_kernel _Z10knn_selectPKiPKfS2_S2_Pf
		.amdhsa_group_segment_fixed_size 6752
		.amdhsa_private_segment_fixed_size 0
		.amdhsa_kernarg_size 40
		.amdhsa_user_sgpr_count 2
		.amdhsa_user_sgpr_dispatch_ptr 0
		.amdhsa_user_sgpr_queue_ptr 0
		.amdhsa_user_sgpr_kernarg_segment_ptr 1
		.amdhsa_user_sgpr_dispatch_id 0
		.amdhsa_user_sgpr_kernarg_preload_length 0
		.amdhsa_user_sgpr_kernarg_preload_offset 0
		.amdhsa_user_sgpr_private_segment_size 0
		.amdhsa_uses_dynamic_stack 0
		.amdhsa_enable_private_segment 0
		.amdhsa_system_sgpr_workgroup_id_x 1
		.amdhsa_system_sgpr_workgroup_id_y 0
		.amdhsa_system_sgpr_workgroup_id_z 0
		.amdhsa_system_sgpr_workgroup_info 0
		.amdhsa_system_vgpr_workitem_id 0
		.amdhsa_next_free_vgpr 124
		.amdhsa_next_free_sgpr 36
		.amdhsa_accum_offset 124
		.amdhsa_reserve_vcc 1
		.amdhsa_float_round_mode_32 0
		.amdhsa_float_round_mode_16_64 0
		.amdhsa_float_denorm_mode_32 3
		.amdhsa_float_denorm_mode_16_64 3
		.amdhsa_dx10_clamp 1
		.amdhsa_ieee_mode 1
		.amdhsa_fp16_overflow 0
		.amdhsa_tg_split 0
		.amdhsa_exception_fp_ieee_invalid_op 0
		.amdhsa_exception_fp_denorm_src 0
		.amdhsa_exception_fp_ieee_div_zero 0
		.amdhsa_exception_fp_ieee_overflow 0
		.amdhsa_exception_fp_ieee_underflow 0
		.amdhsa_exception_fp_ieee_inexact 0
		.amdhsa_exception_int_div_zero 0
	.end_amdhsa_kernel

amdhsa.kernels:
  - .agpr_count:     0
    .args:
      - .actual_access:  read_only
        .address_space:  global
        .offset:         0
        .size:           8
        .value_kind:     global_buffer
      - .actual_access:  write_only
        .address_space:  global
        .offset:         8
        .size:           8
        .value_kind:     global_buffer
      - .actual_access:  read_only
        .address_space:  global
        .offset:         16
        .size:           8
        .value_kind:     global_buffer
      - .actual_access:  write_only
        .address_space:  global
        .offset:         24
        .size:           8
        .value_kind:     global_buffer
    .group_segment_fixed_size: 0
    .kernarg_segment_align: 8
    .kernarg_segment_size: 32
    .language:       OpenCL C
    .language_version:
      - 2
      - 0
    .max_flat_workgroup_size: 512
    .name:           _Z9prep_rowsPKfPcS0_S1_
    .private_segment_fixed_size: 0
    .sgpr_count:     28
    .sgpr_spill_count: 0
    .symbol:         _Z9prep_rowsPKfPcS0_S1_.kd
    .uniform_work_group_size: 1
    .uses_dynamic_stack: false
    .vgpr_count:     50
    .vgpr_spill_count: 0
    .wavefront_size: 64
  - .agpr_count:     0
    .args:
      - .address_space:  global
        .offset:         0
        .size:           8
        .value_kind:     global_buffer
      - .address_space:  global
        .offset:         8
        .size:           8
        .value_kind:     global_buffer
      - .actual_access:  write_only
        .address_space:  global
        .offset:         16
        .size:           8
        .value_kind:     global_buffer
    .group_segment_fixed_size: 0
    .kernarg_segment_align: 8
    .kernarg_segment_size: 24
    .language:       OpenCL C
    .language_version:
      - 2
      - 0
    .max_flat_workgroup_size: 512
    .name:           _Z8knn_gemmPKcS0_Pi
    .private_segment_fixed_size: 0
    .sgpr_count:     78
    .sgpr_spill_count: 0
    .symbol:         _Z8knn_gemmPKcS0_Pi.kd
    .uniform_work_group_size: 1
    .uses_dynamic_stack: false
    .vgpr_count:     232
    .vgpr_spill_count: 0
    .wavefront_size: 64
  - .agpr_count:     0
    .args:
      - .actual_access:  read_only
        .address_space:  global
        .offset:         0
        .size:           8
        .value_kind:     global_buffer
      - .actual_access:  read_only
        .address_space:  global
        .offset:         8
        .size:           8
        .value_kind:     global_buffer
      - .actual_access:  read_only
        .address_space:  global
        .offset:         16
        .size:           8
        .value_kind:     global_buffer
      - .actual_access:  read_only
        .address_space:  global
        .offset:         24
        .size:           8
        .value_kind:     global_buffer
      - .actual_access:  write_only
        .address_space:  global
        .offset:         32
        .size:           8
        .value_kind:     global_buffer
    .group_segment_fixed_size: 6752
    .kernarg_segment_align: 8
    .kernarg_segment_size: 40
    .language:       OpenCL C
    .language_version:
      - 2
      - 0
    .max_flat_workgroup_size: 256
    .name:           _Z10knn_selectPKiPKfS2_S2_Pf
    .private_segment_fixed_size: 0
    .sgpr_count:     42
    .sgpr_spill_count: 0
    .symbol:         _Z10knn_selectPKiPKfS2_S2_Pf.kd
    .uniform_work_group_size: 1
    .uses_dynamic_stack: false
    .vgpr_count:     124
    .vgpr_spill_count: 0
    .wavefront_size: 64
